# QKV K-loop rewritten as register double-buffered pipeline (1 barrier per K-tile, reads + DMA refills interleaved with MFMAs)
# speedup vs baseline: 1.0646x; 1.0043x over previous
.Lqk_bias_done:
	v_lshlrev_b32_e32 v5, 7, v0
	v_lshlrev_b32_e32 v2, 3, v2
	s_mov_b32 s7, 0x1fc00
	v_mov_b32_e32 v6, 0x10000
	s_add_u32 s16, s24, s18
	v_and_b32_e32 v3, 56, v2
	v_and_b32_e32 v4, 0xfc00, v5
	v_bitop3_b32 v5, v5, s7, v6 bitop3:0xc8
	v_lshlrev_b32_e32 v8, 8, v0
	s_mov_b32 s7, 0x3f800
	v_mov_b32_e32 v7, 0x20000
	s_addc_u32 s17, s25, s19
	v_or_b32_e32 v2, v4, v3
	v_bitop3_b32 v7, v8, s7, v7 bitop3:0xc8
	s_mov_b32 s7, 0x7f800
	v_mov_b32_e32 v11, 0x60000
	s_waitcnt lgkmcnt(0)
	s_add_u32 s22, s0, s2
	v_and_b32_e32 v6, 0x1f800, v8
	v_bitop3_b32 v8, v8, s7, v11 bitop3:0xc8
	v_lshlrev_b32_e32 v12, 1, v2
	v_mov_b32_e32 v2, 0
	v_readfirstlane_b32 s7, v79
	v_or_b32_e32 v9, v5, v3
	s_addc_u32 s23, s1, s3
	v_mov_b32_e32 v13, v2
	s_mov_b32 m0, s7
	v_lshl_add_u64 v[14:15], s[22:23], 0, v[12:13]
	global_load_lds_dwordx4 v12, s[22:23]
	v_lshlrev_b32_e32 v12, 1, v9
	v_or_b32_e32 v9, 0x2000, v79
	v_or_b32_e32 v10, v6, v3
	v_readfirstlane_b32 s7, v9
	v_or_b32_e32 v9, 0x4000, v79
	s_mov_b32 m0, s7
	v_readfirstlane_b32 s7, v9
	v_or_b32_e32 v9, 0x6000, v79
	v_or_b32_e32 v18, v7, v3
	v_lshlrev_b32_e32 v10, 1, v10
	global_load_lds_dwordx4 v12, s[22:23]
	s_mov_b32 m0, s7
	v_readfirstlane_b32 s7, v9
	v_or_b32_e32 v9, 0x8000, v79
	v_mov_b32_e32 v11, v2
	global_load_lds_dwordx4 v10, s[16:17]
	v_lshlrev_b32_e32 v18, 1, v18
	s_mov_b32 m0, s7
	v_readfirstlane_b32 s7, v9
	v_or_b32_e32 v9, 0xa000, v79
	v_or_b32_e32 v22, v8, v3
	v_lshl_add_u64 v[16:17], s[22:23], 0, v[12:13]
	v_lshl_add_u64 v[12:13], s[16:17], 0, v[10:11]
	v_mov_b32_e32 v19, v2
	global_load_lds_dwordx4 v18, s[16:17]
	v_or_b32_e32 v10, 0x80000, v10
	s_mov_b32 m0, s7
	v_readfirstlane_b32 s7, v9
	v_lshl_add_u64 v[20:21], s[16:17], 0, v[18:19]
	v_lshl_add_u64 v[18:19], s[16:17], 0, v[10:11]
	global_load_lds_dwordx4 v10, s[16:17]
	v_lshlrev_b32_e32 v10, 1, v22
	s_mov_b32 m0, s7
	v_or_b32_e32 v9, 0xc000, v79
	v_lshl_add_u64 v[22:23], s[16:17], 0, v[10:11]
	global_load_lds_dwordx4 v10, s[16:17]
	s_mov_b64 s[16:17], 0x80
	v_readfirstlane_b32 s7, v9
	v_or_b32_e32 v9, 0xe000, v79
	v_lshl_add_u64 v[10:11], v[14:15], 0, s[16:17]
	s_mov_b32 m0, s7
	v_readfirstlane_b32 s7, v9
	v_or_b32_e32 v9, 0x10000, v79
	global_load_lds_dwordx4 v[10:11], off
	v_lshl_add_u64 v[10:11], v[16:17], 0, s[16:17]
	s_mov_b32 m0, s7
	v_readfirstlane_b32 s7, v9
	v_or_b32_e32 v9, 0x12000, v79
	global_load_lds_dwordx4 v[10:11], off
	v_lshl_add_u64 v[10:11], v[12:13], 0, s[16:17]
	s_mov_b32 m0, s7
	v_readfirstlane_b32 s7, v9
	v_or_b32_e32 v9, 0x14000, v79
	global_load_lds_dwordx4 v[10:11], off
	v_lshl_add_u64 v[10:11], v[20:21], 0, s[16:17]
	s_mov_b32 m0, s7
	v_readfirstlane_b32 s7, v9
	v_or_b32_e32 v9, 0x16000, v79
	global_load_lds_dwordx4 v[10:11], off
	v_lshl_add_u64 v[10:11], v[18:19], 0, s[16:17]
	s_mov_b32 m0, s7
	v_readfirstlane_b32 s7, v9
	global_load_lds_dwordx4 v[10:11], off
	v_lshl_add_u64 v[10:11], v[22:23], 0, s[16:17]
	s_mov_b32 m0, s7
	s_nop 0
	global_load_lds_dwordx4 v[10:11], off
	s_cmp_lt_i32 s20, 16
	s_cselect_b64 s[16:17], -1, 0
	s_cmp_gt_i32 s20, 15
	v_bfe_u32 v9, v0, 6, 2
	s_cselect_b64 vcc, -1, 0
	v_cndmask_b32_e32 v83, v78, v9, vcc
	v_cndmask_b32_e32 v9, v9, v78, vcc
	s_and_b64 s[22:23], vcc, exec
	v_lshl_or_b32 v80, v9, 6, v42
	v_bfe_u32 v9, v0, 1, 3
	s_cselect_b32 s26, 0x2000, 0
	s_cselect_b32 s27, 0, 0x2000
	v_bitop3_b32 v9, v1, v9, 4 bitop3:0x36
	s_add_u32 s18, s24, s18
	v_lshlrev_b32_e32 v84, 4, v9
	v_add_lshl_u32 v8, v8, v3, 1
	v_mov_b32_e32 v9, v2
	s_addc_u32 s19, s25, s19
	v_lshl_add_u64 v[8:9], s[18:19], 0, v[8:9]
	s_mov_b64 s[22:23], 0x100
	v_lshl_add_u64 v[66:67], v[8:9], 0, s[22:23]
	v_add_lshl_u32 v8, v7, v3, 1
	v_mov_b32_e32 v9, v2
	v_lshl_add_u64 v[8:9], s[18:19], 0, v[8:9]
	v_add_lshl_u32 v6, v6, v3, 1
	v_mov_b32_e32 v7, v2
	v_lshl_add_u64 v[68:69], v[8:9], 0, s[22:23]
	v_lshl_add_u64 v[8:9], s[18:19], 0, v[6:7]
	v_or_b32_e32 v6, 0x80000, v6
	v_lshlrev_b32_e32 v82, 6, v83
	v_lshl_add_u64 v[6:7], s[18:19], 0, v[6:7]
	s_add_u32 s0, s0, s2
	v_or_b32_e32 v10, v82, v42
	v_lshl_add_u64 v[72:73], v[6:7], 0, s[22:23]
	v_add_lshl_u32 v6, v5, v3, 1
	v_mov_b32_e32 v7, v2
	s_addc_u32 s1, s1, s3
	v_add_lshl_u32 v4, v4, v3, 1
	v_mov_b32_e32 v5, v2
	v_lshlrev_b32_e32 v86, 7, v10
	v_bitop3_b32 v10, v43, v1, 7 bitop3:0x6c
	v_lshl_add_u64 v[6:7], s[0:1], 0, v[6:7]
	v_lshl_add_u64 v[4:5], s[0:1], 0, v[4:5]
	v_lshlrev_b32_e32 v85, 4, v10
	v_lshlrev_b32_e32 v81, 7, v80
	v_lshl_add_u64 v[70:71], v[8:9], 0, s[22:23]
	v_lshl_add_u64 v[74:75], v[6:7], 0, s[22:23]
	v_lshl_add_u64 v[76:77], v[4:5], 0, s[22:23]
	s_mov_b32 s18, 2
	s_mov_b64 s[0:1], 0
	s_lshl_b32 s3, s26, 1
	s_lshl_b32 s2, s27, 1
	v_mov_b32_e32 v3, v2
	v_mov_b32_e32 v4, v2
	v_mov_b32_e32 v5, v2
	v_mov_b32_e32 v6, v2
	v_mov_b32_e32 v7, v2
	v_mov_b32_e32 v8, v2
	v_mov_b32_e32 v9, v2
	v_mov_b32_e32 v10, v2
	v_mov_b32_e32 v11, v2
	v_mov_b32_e32 v12, v2
	v_mov_b32_e32 v13, v2
	v_mov_b32_e32 v14, v2
	v_mov_b32_e32 v15, v2
	v_mov_b32_e32 v16, v2
	v_mov_b32_e32 v17, v2
	v_mov_b32_e32 v18, v2
	v_mov_b32_e32 v19, v2
	v_mov_b32_e32 v20, v2
	v_mov_b32_e32 v21, v2
	v_mov_b32_e32 v22, v2
	v_mov_b32_e32 v23, v2
	v_mov_b32_e32 v24, v2
	v_mov_b32_e32 v25, v2
	v_mov_b32_e32 v26, v2
	v_mov_b32_e32 v27, v2
	v_mov_b32_e32 v28, v2
	v_mov_b32_e32 v29, v2
	v_mov_b32_e32 v30, v2
	v_mov_b32_e32 v31, v2
	v_mov_b32_e32 v32, v2
	v_mov_b32_e32 v33, v2
	v_mov_b32_e32 v34, v2
	v_mov_b32_e32 v35, v2
	v_mov_b32_e32 v36, v2
	v_mov_b32_e32 v37, v2
	v_mov_b32_e32 v38, v2
	v_mov_b32_e32 v39, v2
	v_mov_b32_e32 v40, v2
	v_mov_b32_e32 v41, v2
	v_mov_b32_e32 v42, v2
	v_mov_b32_e32 v43, v2
	v_mov_b32_e32 v44, v2
	v_mov_b32_e32 v45, v2
	v_mov_b32_e32 v46, v2
	v_mov_b32_e32 v47, v2
	v_mov_b32_e32 v48, v2
	v_mov_b32_e32 v49, v2
	v_mov_b32_e32 v50, v2
	v_mov_b32_e32 v51, v2
	v_mov_b32_e32 v52, v2
	v_mov_b32_e32 v53, v2
	v_mov_b32_e32 v54, v2
	v_mov_b32_e32 v55, v2
	v_mov_b32_e32 v56, v2
	v_mov_b32_e32 v57, v2
	v_mov_b32_e32 v58, v2
	v_mov_b32_e32 v59, v2
	v_mov_b32_e32 v60, v2
	v_mov_b32_e32 v61, v2
	v_mov_b32_e32 v62, v2
	v_mov_b32_e32 v63, v2
	v_mov_b32_e32 v64, v2
	v_mov_b32_e32 v65, v2
	v_readfirstlane_b32 s44, v79
	s_mov_b32 s45, 0
	s_mov_b32 s46, 1
	s_mov_b32 s48, 0
	s_mov_b64 s[0:1], 0
	s_add_u32 s49, s44, 0x18000
	s_mov_b32 m0, s49
	v_lshl_add_u64 v[124:125], v[76:77], 0, s[0:1]
	global_load_lds_dwordx4 v[124:125], off
	s_add_u32 m0, s49, 0x2000
	v_lshl_add_u64 v[124:125], v[74:75], 0, s[0:1]
	global_load_lds_dwordx4 v[124:125], off
	s_add_u32 m0, s49, 0x4000
	v_lshl_add_u64 v[124:125], v[70:71], 0, s[0:1]
	global_load_lds_dwordx4 v[124:125], off
	s_add_u32 m0, s49, 0x6000
	v_lshl_add_u64 v[124:125], v[68:69], 0, s[0:1]
	global_load_lds_dwordx4 v[124:125], off
	s_add_u32 m0, s49, 0x8000
	v_lshl_add_u64 v[124:125], v[72:73], 0, s[0:1]
	global_load_lds_dwordx4 v[124:125], off
	s_add_u32 m0, s49, 0xa000
	v_lshl_add_u64 v[124:125], v[66:67], 0, s[0:1]
	global_load_lds_dwordx4 v[124:125], off
	s_mov_b64 s[0:1], 0x80
	s_waitcnt vmcnt(12)
	s_barrier
	s_mov_b32 s46, 0
	s_mul_i32 s49, s46, 0xc000
	s_add_u32 s50, s49, s3
	s_add_u32 s51, s49, s2
	v_add3_u32 v120, s50, v86, v85
	v_add3_u32 v121, s50, v86, v84
	v_add3_u32 v122, s51, v81, v85
	v_add3_u32 v123, s51, v81, v84
	ds_read_b128 v[88:91], v120
	ds_read_b128 v[92:95], v120 offset:2048
	ds_read_b128 v[96:99], v120 offset:4096
	ds_read_b128 v[100:103], v120 offset:6144
	ds_read_b128 v[104:107], v122
	ds_read_b128 v[108:111], v122 offset:2048
	ds_read_b128 v[112:115], v122 offset:4096
	ds_read_b128 v[116:119], v122 offset:6144
	ds_read_b128 v[144:147], v121
	ds_read_b128 v[148:151], v121 offset:2048
	ds_read_b128 v[152:155], v121 offset:4096
	ds_read_b128 v[156:159], v121 offset:6144
	ds_read_b128 v[160:163], v123
	ds_read_b128 v[164:167], v123 offset:2048
	ds_read_b128 v[168:171], v123 offset:4096
	ds_read_b128 v[172:175], v123 offset:6144
	s_mov_b32 s46, 1
.LBB1_36:
	s_waitcnt vmcnt(6)
	s_waitcnt lgkmcnt(0)
	s_barrier
	s_mul_i32 s49, s46, 0xc000
	s_add_u32 s50, s49, s3
	s_add_u32 s51, s49, s2
	v_add3_u32 v120, s50, v86, v85
	v_add3_u32 v121, s50, v86, v84
	v_add3_u32 v122, s51, v81, v85
	v_add3_u32 v123, s51, v81, v84
	s_mul_i32 s49, s45, 0xc000
	s_add_u32 s49, s49, s44
	s_setprio 1
	ds_read_b128 v[176:179], v120
	ds_read_b128 v[180:183], v120 offset:2048
	ds_read_b128 v[184:187], v120 offset:4096
	ds_read_b128 v[188:191], v120 offset:6144
	v_mfma_f32_16x16x32_f16 v[62:65], v[88:91], v[104:107], v[62:65]
	ds_read_b128 v[192:195], v122
	v_mfma_f32_16x16x32_f16 v[58:61], v[88:91], v[108:111], v[58:61]
	ds_read_b128 v[196:199], v122 offset:2048
	v_mfma_f32_16x16x32_f16 v[54:57], v[88:91], v[112:115], v[54:57]
	ds_read_b128 v[200:203], v122 offset:4096
	v_mfma_f32_16x16x32_f16 v[50:53], v[88:91], v[116:119], v[50:53]
	ds_read_b128 v[204:207], v122 offset:6144
	v_mfma_f32_16x16x32_f16 v[46:49], v[92:95], v[104:107], v[46:49]
	ds_read_b128 v[208:211], v121
	v_mfma_f32_16x16x32_f16 v[42:45], v[92:95], v[108:111], v[42:45]
	ds_read_b128 v[212:215], v121 offset:2048
	v_mfma_f32_16x16x32_f16 v[38:41], v[92:95], v[112:115], v[38:41]
	ds_read_b128 v[216:219], v121 offset:4096
	v_mfma_f32_16x16x32_f16 v[34:37], v[92:95], v[116:119], v[34:37]
	ds_read_b128 v[220:223], v121 offset:6144
	v_mfma_f32_16x16x32_f16 v[30:33], v[96:99], v[104:107], v[30:33]
	ds_read_b128 v[224:227], v123
	v_mfma_f32_16x16x32_f16 v[26:29], v[96:99], v[108:111], v[26:29]
	ds_read_b128 v[228:231], v123 offset:2048
	v_mfma_f32_16x16x32_f16 v[22:25], v[96:99], v[112:115], v[22:25]
	ds_read_b128 v[232:235], v123 offset:4096
	v_mfma_f32_16x16x32_f16 v[18:21], v[96:99], v[116:119], v[18:21]
	ds_read_b128 v[236:239], v123 offset:6144
	v_mfma_f32_16x16x32_f16 v[14:17], v[100:103], v[104:107], v[14:17]
	v_mfma_f32_16x16x32_f16 v[10:13], v[100:103], v[108:111], v[10:13]
	v_mfma_f32_16x16x32_f16 v[6:9], v[100:103], v[112:115], v[6:9]
	s_mov_b32 m0, s49
	v_lshl_add_u64 v[124:125], v[76:77], 0, s[0:1]
	global_load_lds_dwordx4 v[124:125], off
	v_mfma_f32_16x16x32_f16 v[2:5], v[100:103], v[116:119], v[2:5]
	v_mfma_f32_16x16x32_f16 v[62:65], v[144:147], v[160:163], v[62:65]
	v_mfma_f32_16x16x32_f16 v[58:61], v[144:147], v[164:167], v[58:61]
	s_add_u32 m0, s49, 0x2000
	v_lshl_add_u64 v[124:125], v[74:75], 0, s[0:1]
	global_load_lds_dwordx4 v[124:125], off
	v_mfma_f32_16x16x32_f16 v[54:57], v[144:147], v[168:171], v[54:57]
	v_mfma_f32_16x16x32_f16 v[50:53], v[144:147], v[172:175], v[50:53]
	v_mfma_f32_16x16x32_f16 v[46:49], v[148:151], v[160:163], v[46:49]
	s_add_u32 m0, s49, 0x4000
	v_lshl_add_u64 v[124:125], v[70:71], 0, s[0:1]
	global_load_lds_dwordx4 v[124:125], off
	v_mfma_f32_16x16x32_f16 v[42:45], v[148:151], v[164:167], v[42:45]
	v_mfma_f32_16x16x32_f16 v[38:41], v[148:151], v[168:171], v[38:41]
	v_mfma_f32_16x16x32_f16 v[34:37], v[148:151], v[172:175], v[34:37]
	s_add_u32 m0, s49, 0x6000
	v_lshl_add_u64 v[124:125], v[68:69], 0, s[0:1]
	global_load_lds_dwordx4 v[124:125], off
	v_mfma_f32_16x16x32_f16 v[30:33], v[152:155], v[160:163], v[30:33]
	v_mfma_f32_16x16x32_f16 v[26:29], v[152:155], v[164:167], v[26:29]
	v_mfma_f32_16x16x32_f16 v[22:25], v[152:155], v[168:171], v[22:25]
	s_add_u32 m0, s49, 0x8000
	v_lshl_add_u64 v[124:125], v[72:73], 0, s[0:1]
	global_load_lds_dwordx4 v[124:125], off
	v_mfma_f32_16x16x32_f16 v[18:21], v[152:155], v[172:175], v[18:21]
	v_mfma_f32_16x16x32_f16 v[14:17], v[156:159], v[160:163], v[14:17]
	v_mfma_f32_16x16x32_f16 v[10:13], v[156:159], v[164:167], v[10:13]
	s_add_u32 m0, s49, 0xa000
	v_lshl_add_u64 v[124:125], v[66:67], 0, s[0:1]
	global_load_lds_dwordx4 v[124:125], off
	v_mfma_f32_16x16x32_f16 v[6:9], v[156:159], v[168:171], v[6:9]
	v_mfma_f32_16x16x32_f16 v[2:5], v[156:159], v[172:175], v[2:5]
	s_setprio 0
	s_add_u32 s0, s0, 0x80
	s_addc_u32 s1, s1, 0
	s_add_i32 s48, s48, 1
	s_add_i32 s49, s45, 1
	s_cmp_lg_u32 s45, 2
	s_cselect_b32 s45, s49, 0
	s_add_i32 s49, s46, 1
	s_cmp_lg_u32 s46, 2
	s_cselect_b32 s46, s49, 0
	s_waitcnt vmcnt(6)
	s_waitcnt lgkmcnt(0)
	s_barrier
	s_mul_i32 s49, s46, 0xc000
	s_add_u32 s50, s49, s3
	s_add_u32 s51, s49, s2
	v_add3_u32 v120, s50, v86, v85
	v_add3_u32 v121, s50, v86, v84
	v_add3_u32 v122, s51, v81, v85
	v_add3_u32 v123, s51, v81, v84
	s_mul_i32 s49, s45, 0xc000
	s_add_u32 s49, s49, s44
	s_setprio 1
	ds_read_b128 v[88:91], v120
	ds_read_b128 v[92:95], v120 offset:2048
	ds_read_b128 v[96:99], v120 offset:4096
	ds_read_b128 v[100:103], v120 offset:6144
	v_mfma_f32_16x16x32_f16 v[62:65], v[176:179], v[192:195], v[62:65]
	ds_read_b128 v[104:107], v122
	v_mfma_f32_16x16x32_f16 v[58:61], v[176:179], v[196:199], v[58:61]
	ds_read_b128 v[108:111], v122 offset:2048
	v_mfma_f32_16x16x32_f16 v[54:57], v[176:179], v[200:203], v[54:57]
	ds_read_b128 v[112:115], v122 offset:4096
	v_mfma_f32_16x16x32_f16 v[50:53], v[176:179], v[204:207], v[50:53]
	ds_read_b128 v[116:119], v122 offset:6144
	v_mfma_f32_16x16x32_f16 v[46:49], v[180:183], v[192:195], v[46:49]
	ds_read_b128 v[144:147], v121
	v_mfma_f32_16x16x32_f16 v[42:45], v[180:183], v[196:199], v[42:45]
	ds_read_b128 v[148:151], v121 offset:2048
	v_mfma_f32_16x16x32_f16 v[38:41], v[180:183], v[200:203], v[38:41]
	ds_read_b128 v[152:155], v121 offset:4096
	v_mfma_f32_16x16x32_f16 v[34:37], v[180:183], v[204:207], v[34:37]
	ds_read_b128 v[156:159], v121 offset:6144
	v_mfma_f32_16x16x32_f16 v[30:33], v[184:187], v[192:195], v[30:33]
	ds_read_b128 v[160:163], v123
	v_mfma_f32_16x16x32_f16 v[26:29], v[184:187], v[196:199], v[26:29]
	ds_read_b128 v[164:167], v123 offset:2048
	v_mfma_f32_16x16x32_f16 v[22:25], v[184:187], v[200:203], v[22:25]
	ds_read_b128 v[168:171], v123 offset:4096
	v_mfma_f32_16x16x32_f16 v[18:21], v[184:187], v[204:207], v[18:21]
	ds_read_b128 v[172:175], v123 offset:6144
	v_mfma_f32_16x16x32_f16 v[14:17], v[188:191], v[192:195], v[14:17]
	v_mfma_f32_16x16x32_f16 v[10:13], v[188:191], v[196:199], v[10:13]
	v_mfma_f32_16x16x32_f16 v[6:9], v[188:191], v[200:203], v[6:9]
	s_mov_b32 m0, s49
	v_lshl_add_u64 v[124:125], v[76:77], 0, s[0:1]
	global_load_lds_dwordx4 v[124:125], off
	v_mfma_f32_16x16x32_f16 v[2:5], v[188:191], v[204:207], v[2:5]
	v_mfma_f32_16x16x32_f16 v[62:65], v[208:211], v[224:227], v[62:65]
	v_mfma_f32_16x16x32_f16 v[58:61], v[208:211], v[228:231], v[58:61]
	s_add_u32 m0, s49, 0x2000
	v_lshl_add_u64 v[124:125], v[74:75], 0, s[0:1]
	global_load_lds_dwordx4 v[124:125], off
	v_mfma_f32_16x16x32_f16 v[54:57], v[208:211], v[232:235], v[54:57]
	v_mfma_f32_16x16x32_f16 v[50:53], v[208:211], v[236:239], v[50:53]
	v_mfma_f32_16x16x32_f16 v[46:49], v[212:215], v[224:227], v[46:49]
	s_add_u32 m0, s49, 0x4000
	v_lshl_add_u64 v[124:125], v[70:71], 0, s[0:1]
	global_load_lds_dwordx4 v[124:125], off
	v_mfma_f32_16x16x32_f16 v[42:45], v[212:215], v[228:231], v[42:45]
	v_mfma_f32_16x16x32_f16 v[38:41], v[212:215], v[232:235], v[38:41]
	v_mfma_f32_16x16x32_f16 v[34:37], v[212:215], v[236:239], v[34:37]
	s_add_u32 m0, s49, 0x6000
	v_lshl_add_u64 v[124:125], v[68:69], 0, s[0:1]
	global_load_lds_dwordx4 v[124:125], off
	v_mfma_f32_16x16x32_f16 v[30:33], v[216:219], v[224:227], v[30:33]
	v_mfma_f32_16x16x32_f16 v[26:29], v[216:219], v[228:231], v[26:29]
	v_mfma_f32_16x16x32_f16 v[22:25], v[216:219], v[232:235], v[22:25]
	s_add_u32 m0, s49, 0x8000
	v_lshl_add_u64 v[124:125], v[72:73], 0, s[0:1]
	global_load_lds_dwordx4 v[124:125], off
	v_mfma_f32_16x16x32_f16 v[18:21], v[216:219], v[236:239], v[18:21]
	v_mfma_f32_16x16x32_f16 v[14:17], v[220:223], v[224:227], v[14:17]
	v_mfma_f32_16x16x32_f16 v[10:13], v[220:223], v[228:231], v[10:13]
	s_add_u32 m0, s49, 0xa000
	v_lshl_add_u64 v[124:125], v[66:67], 0, s[0:1]
	global_load_lds_dwordx4 v[124:125], off
	v_mfma_f32_16x16x32_f16 v[6:9], v[220:223], v[232:235], v[6:9]
	v_mfma_f32_16x16x32_f16 v[2:5], v[220:223], v[236:239], v[2:5]
	s_setprio 0
	s_add_u32 s0, s0, 0x80
	s_addc_u32 s1, s1, 0
	s_add_i32 s48, s48, 1
	s_add_i32 s49, s45, 1
	s_cmp_lg_u32 s45, 2
	s_cselect_b32 s45, s49, 0
	s_add_i32 s49, s46, 1
	s_cmp_lg_u32 s46, 2
	s_cselect_b32 s46, s49, 0
	s_cmp_lt_u32 s48, 12
	s_cbranch_scc1 .LBB1_36
	s_waitcnt vmcnt(6)
	s_waitcnt lgkmcnt(0)
	s_barrier
	s_mul_i32 s49, s46, 0xc000
	s_add_u32 s50, s49, s3
	s_add_u32 s51, s49, s2
	v_add3_u32 v120, s50, v86, v85
	v_add3_u32 v121, s50, v86, v84
	v_add3_u32 v122, s51, v81, v85
	v_add3_u32 v123, s51, v81, v84
	s_mul_i32 s49, s45, 0xc000
	s_add_u32 s49, s49, s44
	s_setprio 1
	ds_read_b128 v[176:179], v120
	ds_read_b128 v[180:183], v120 offset:2048
	ds_read_b128 v[184:187], v120 offset:4096
	ds_read_b128 v[188:191], v120 offset:6144
	v_mfma_f32_16x16x32_f16 v[62:65], v[88:91], v[104:107], v[62:65]
	ds_read_b128 v[192:195], v122
	v_mfma_f32_16x16x32_f16 v[58:61], v[88:91], v[108:111], v[58:61]
	ds_read_b128 v[196:199], v122 offset:2048
	v_mfma_f32_16x16x32_f16 v[54:57], v[88:91], v[112:115], v[54:57]
	ds_read_b128 v[200:203], v122 offset:4096
	v_mfma_f32_16x16x32_f16 v[50:53], v[88:91], v[116:119], v[50:53]
	ds_read_b128 v[204:207], v122 offset:6144
	v_mfma_f32_16x16x32_f16 v[46:49], v[92:95], v[104:107], v[46:49]
	ds_read_b128 v[208:211], v121
	v_mfma_f32_16x16x32_f16 v[42:45], v[92:95], v[108:111], v[42:45]
	ds_read_b128 v[212:215], v121 offset:2048
	v_mfma_f32_16x16x32_f16 v[38:41], v[92:95], v[112:115], v[38:41]
	ds_read_b128 v[216:219], v121 offset:4096
	v_mfma_f32_16x16x32_f16 v[34:37], v[92:95], v[116:119], v[34:37]
	ds_read_b128 v[220:223], v121 offset:6144
	v_mfma_f32_16x16x32_f16 v[30:33], v[96:99], v[104:107], v[30:33]
	ds_read_b128 v[224:227], v123
	v_mfma_f32_16x16x32_f16 v[26:29], v[96:99], v[108:111], v[26:29]
	ds_read_b128 v[228:231], v123 offset:2048
	v_mfma_f32_16x16x32_f16 v[22:25], v[96:99], v[112:115], v[22:25]
	ds_read_b128 v[232:235], v123 offset:4096
	v_mfma_f32_16x16x32_f16 v[18:21], v[96:99], v[116:119], v[18:21]
	ds_read_b128 v[236:239], v123 offset:6144
	v_mfma_f32_16x16x32_f16 v[14:17], v[100:103], v[104:107], v[14:17]
	v_mfma_f32_16x16x32_f16 v[10:13], v[100:103], v[108:111], v[10:13]
	v_mfma_f32_16x16x32_f16 v[6:9], v[100:103], v[112:115], v[6:9]
	s_mov_b32 m0, s49
	v_lshl_add_u64 v[124:125], v[76:77], 0, s[0:1]
	global_load_lds_dwordx4 v[124:125], off
	v_mfma_f32_16x16x32_f16 v[2:5], v[100:103], v[116:119], v[2:5]
	v_mfma_f32_16x16x32_f16 v[62:65], v[144:147], v[160:163], v[62:65]
	v_mfma_f32_16x16x32_f16 v[58:61], v[144:147], v[164:167], v[58:61]
	s_add_u32 m0, s49, 0x2000
	v_lshl_add_u64 v[124:125], v[74:75], 0, s[0:1]
	global_load_lds_dwordx4 v[124:125], off
	v_mfma_f32_16x16x32_f16 v[54:57], v[144:147], v[168:171], v[54:57]
	v_mfma_f32_16x16x32_f16 v[50:53], v[144:147], v[172:175], v[50:53]
	v_mfma_f32_16x16x32_f16 v[46:49], v[148:151], v[160:163], v[46:49]
	s_add_u32 m0, s49, 0x4000
	v_lshl_add_u64 v[124:125], v[70:71], 0, s[0:1]
	global_load_lds_dwordx4 v[124:125], off
	v_mfma_f32_16x16x32_f16 v[42:45], v[148:151], v[164:167], v[42:45]
	v_mfma_f32_16x16x32_f16 v[38:41], v[148:151], v[168:171], v[38:41]
	v_mfma_f32_16x16x32_f16 v[34:37], v[148:151], v[172:175], v[34:37]
	s_add_u32 m0, s49, 0x6000
	v_lshl_add_u64 v[124:125], v[68:69], 0, s[0:1]
	global_load_lds_dwordx4 v[124:125], off
	v_mfma_f32_16x16x32_f16 v[30:33], v[152:155], v[160:163], v[30:33]
	v_mfma_f32_16x16x32_f16 v[26:29], v[152:155], v[164:167], v[26:29]
	v_mfma_f32_16x16x32_f16 v[22:25], v[152:155], v[168:171], v[22:25]
	s_add_u32 m0, s49, 0x8000
	v_lshl_add_u64 v[124:125], v[72:73], 0, s[0:1]
	global_load_lds_dwordx4 v[124:125], off
	v_mfma_f32_16x16x32_f16 v[18:21], v[152:155], v[172:175], v[18:21]
	v_mfma_f32_16x16x32_f16 v[14:17], v[156:159], v[160:163], v[14:17]
	v_mfma_f32_16x16x32_f16 v[10:13], v[156:159], v[164:167], v[10:13]
	s_add_u32 m0, s49, 0xa000
	v_lshl_add_u64 v[124:125], v[66:67], 0, s[0:1]
	global_load_lds_dwordx4 v[124:125], off
	v_mfma_f32_16x16x32_f16 v[6:9], v[156:159], v[168:171], v[6:9]
	v_mfma_f32_16x16x32_f16 v[2:5], v[156:159], v[172:175], v[2:5]
	s_setprio 0
	s_add_u32 s0, s0, 0x80
	s_addc_u32 s1, s1, 0
	s_add_i32 s48, s48, 1
	s_add_i32 s49, s45, 1
	s_cmp_lg_u32 s45, 2
	s_cselect_b32 s45, s49, 0
	s_add_i32 s49, s46, 1
	s_cmp_lg_u32 s46, 2
	s_cselect_b32 s46, s49, 0
	s_waitcnt vmcnt(6)
	s_waitcnt lgkmcnt(0)
	s_barrier
	s_mul_i32 s49, s46, 0xc000
	s_add_u32 s50, s49, s3
	s_add_u32 s51, s49, s2
	v_add3_u32 v120, s50, v86, v85
	v_add3_u32 v121, s50, v86, v84
	v_add3_u32 v122, s51, v81, v85
	v_add3_u32 v123, s51, v81, v84
	s_setprio 1
	ds_read_b128 v[88:91], v120
	ds_read_b128 v[92:95], v120 offset:2048
	ds_read_b128 v[96:99], v120 offset:4096
	ds_read_b128 v[100:103], v120 offset:6144
	v_mfma_f32_16x16x32_f16 v[62:65], v[176:179], v[192:195], v[62:65]
	ds_read_b128 v[104:107], v122
	v_mfma_f32_16x16x32_f16 v[58:61], v[176:179], v[196:199], v[58:61]
	ds_read_b128 v[108:111], v122 offset:2048
	v_mfma_f32_16x16x32_f16 v[54:57], v[176:179], v[200:203], v[54:57]
	ds_read_b128 v[112:115], v122 offset:4096
	v_mfma_f32_16x16x32_f16 v[50:53], v[176:179], v[204:207], v[50:53]
	ds_read_b128 v[116:119], v122 offset:6144
	v_mfma_f32_16x16x32_f16 v[46:49], v[180:183], v[192:195], v[46:49]
	ds_read_b128 v[144:147], v121
	v_mfma_f32_16x16x32_f16 v[42:45], v[180:183], v[196:199], v[42:45]
	ds_read_b128 v[148:151], v121 offset:2048
	v_mfma_f32_16x16x32_f16 v[38:41], v[180:183], v[200:203], v[38:41]
	ds_read_b128 v[152:155], v121 offset:4096
	v_mfma_f32_16x16x32_f16 v[34:37], v[180:183], v[204:207], v[34:37]
	ds_read_b128 v[156:159], v121 offset:6144
	v_mfma_f32_16x16x32_f16 v[30:33], v[184:187], v[192:195], v[30:33]
	ds_read_b128 v[160:163], v123
	v_mfma_f32_16x16x32_f16 v[26:29], v[184:187], v[196:199], v[26:29]
	ds_read_b128 v[164:167], v123 offset:2048
	v_mfma_f32_16x16x32_f16 v[22:25], v[184:187], v[200:203], v[22:25]
	ds_read_b128 v[168:171], v123 offset:4096
	v_mfma_f32_16x16x32_f16 v[18:21], v[184:187], v[204:207], v[18:21]
	ds_read_b128 v[172:175], v123 offset:6144
	v_mfma_f32_16x16x32_f16 v[14:17], v[188:191], v[192:195], v[14:17]
	v_mfma_f32_16x16x32_f16 v[10:13], v[188:191], v[196:199], v[10:13]
	v_mfma_f32_16x16x32_f16 v[6:9], v[188:191], v[200:203], v[6:9]
	v_mfma_f32_16x16x32_f16 v[2:5], v[188:191], v[204:207], v[2:5]
	v_mfma_f32_16x16x32_f16 v[62:65], v[208:211], v[224:227], v[62:65]
	v_mfma_f32_16x16x32_f16 v[58:61], v[208:211], v[228:231], v[58:61]
	v_mfma_f32_16x16x32_f16 v[54:57], v[208:211], v[232:235], v[54:57]
	v_mfma_f32_16x16x32_f16 v[50:53], v[208:211], v[236:239], v[50:53]
	v_mfma_f32_16x16x32_f16 v[46:49], v[212:215], v[224:227], v[46:49]
	v_mfma_f32_16x16x32_f16 v[42:45], v[212:215], v[228:231], v[42:45]
	v_mfma_f32_16x16x32_f16 v[38:41], v[212:215], v[232:235], v[38:41]
	v_mfma_f32_16x16x32_f16 v[34:37], v[212:215], v[236:239], v[34:37]
	v_mfma_f32_16x16x32_f16 v[30:33], v[216:219], v[224:227], v[30:33]
	v_mfma_f32_16x16x32_f16 v[26:29], v[216:219], v[228:231], v[26:29]
	v_mfma_f32_16x16x32_f16 v[22:25], v[216:219], v[232:235], v[22:25]
	v_mfma_f32_16x16x32_f16 v[18:21], v[216:219], v[236:239], v[18:21]
	v_mfma_f32_16x16x32_f16 v[14:17], v[220:223], v[224:227], v[14:17]
	v_mfma_f32_16x16x32_f16 v[10:13], v[220:223], v[228:231], v[10:13]
	v_mfma_f32_16x16x32_f16 v[6:9], v[220:223], v[232:235], v[6:9]
	v_mfma_f32_16x16x32_f16 v[2:5], v[220:223], v[236:239], v[2:5]
	s_setprio 0
	s_add_u32 s0, s0, 0x80
	s_addc_u32 s1, s1, 0
	s_add_i32 s48, s48, 1
	s_add_i32 s49, s45, 1
	s_cmp_lg_u32 s45, 2
	s_cselect_b32 s45, s49, 0
	s_add_i32 s49, s46, 1
	s_cmp_lg_u32 s46, 2
	s_cselect_b32 s46, s49, 0
	s_waitcnt vmcnt(0)
	s_waitcnt lgkmcnt(0)
	s_barrier
	s_mul_i32 s49, s46, 0xc000
	s_add_u32 s50, s49, s3
	s_add_u32 s51, s49, s2
	v_add3_u32 v120, s50, v86, v85
	v_add3_u32 v121, s50, v86, v84
	v_add3_u32 v122, s51, v81, v85
	v_add3_u32 v123, s51, v81, v84
	s_setprio 1
	ds_read_b128 v[176:179], v120
	ds_read_b128 v[180:183], v120 offset:2048
	ds_read_b128 v[184:187], v120 offset:4096
	ds_read_b128 v[188:191], v120 offset:6144
	v_mfma_f32_16x16x32_f16 v[62:65], v[88:91], v[104:107], v[62:65]
	ds_read_b128 v[192:195], v122
	v_mfma_f32_16x16x32_f16 v[58:61], v[88:91], v[108:111], v[58:61]
	ds_read_b128 v[196:199], v122 offset:2048
	v_mfma_f32_16x16x32_f16 v[54:57], v[88:91], v[112:115], v[54:57]
	ds_read_b128 v[200:203], v122 offset:4096
	v_mfma_f32_16x16x32_f16 v[50:53], v[88:91], v[116:119], v[50:53]
	ds_read_b128 v[204:207], v122 offset:6144
	v_mfma_f32_16x16x32_f16 v[46:49], v[92:95], v[104:107], v[46:49]
	ds_read_b128 v[208:211], v121
	v_mfma_f32_16x16x32_f16 v[42:45], v[92:95], v[108:111], v[42:45]
	ds_read_b128 v[212:215], v121 offset:2048
	v_mfma_f32_16x16x32_f16 v[38:41], v[92:95], v[112:115], v[38:41]
	ds_read_b128 v[216:219], v121 offset:4096
	v_mfma_f32_16x16x32_f16 v[34:37], v[92:95], v[116:119], v[34:37]
	ds_read_b128 v[220:223], v121 offset:6144
	v_mfma_f32_16x16x32_f16 v[30:33], v[96:99], v[104:107], v[30:33]
	ds_read_b128 v[224:227], v123
	v_mfma_f32_16x16x32_f16 v[26:29], v[96:99], v[108:111], v[26:29]
	ds_read_b128 v[228:231], v123 offset:2048
	v_mfma_f32_16x16x32_f16 v[22:25], v[96:99], v[112:115], v[22:25]
	ds_read_b128 v[232:235], v123 offset:4096
	v_mfma_f32_16x16x32_f16 v[18:21], v[96:99], v[116:119], v[18:21]
	ds_read_b128 v[236:239], v123 offset:6144
	v_mfma_f32_16x16x32_f16 v[14:17], v[100:103], v[104:107], v[14:17]
	v_mfma_f32_16x16x32_f16 v[10:13], v[100:103], v[108:111], v[10:13]
	v_mfma_f32_16x16x32_f16 v[6:9], v[100:103], v[112:115], v[6:9]
	v_mfma_f32_16x16x32_f16 v[2:5], v[100:103], v[116:119], v[2:5]
	v_mfma_f32_16x16x32_f16 v[62:65], v[144:147], v[160:163], v[62:65]
	v_mfma_f32_16x16x32_f16 v[58:61], v[144:147], v[164:167], v[58:61]
	v_mfma_f32_16x16x32_f16 v[54:57], v[144:147], v[168:171], v[54:57]
	v_mfma_f32_16x16x32_f16 v[50:53], v[144:147], v[172:175], v[50:53]
	v_mfma_f32_16x16x32_f16 v[46:49], v[148:151], v[160:163], v[46:49]
	v_mfma_f32_16x16x32_f16 v[42:45], v[148:151], v[164:167], v[42:45]
	v_mfma_f32_16x16x32_f16 v[38:41], v[148:151], v[168:171], v[38:41]
	v_mfma_f32_16x16x32_f16 v[34:37], v[148:151], v[172:175], v[34:37]
	v_mfma_f32_16x16x32_f16 v[30:33], v[152:155], v[160:163], v[30:33]
	v_mfma_f32_16x16x32_f16 v[26:29], v[152:155], v[164:167], v[26:29]
	v_mfma_f32_16x16x32_f16 v[22:25], v[152:155], v[168:171], v[22:25]
	v_mfma_f32_16x16x32_f16 v[18:21], v[152:155], v[172:175], v[18:21]
	v_mfma_f32_16x16x32_f16 v[14:17], v[156:159], v[160:163], v[14:17]
	v_mfma_f32_16x16x32_f16 v[10:13], v[156:159], v[164:167], v[10:13]
	v_mfma_f32_16x16x32_f16 v[6:9], v[156:159], v[168:171], v[6:9]
	v_mfma_f32_16x16x32_f16 v[2:5], v[156:159], v[172:175], v[2:5]
	s_setprio 0
	s_add_u32 s0, s0, 0x80
	s_addc_u32 s1, s1, 0
	s_add_i32 s48, s48, 1
	s_add_i32 s49, s45, 1
	s_cmp_lg_u32 s45, 2
	s_cselect_b32 s45, s49, 0
	s_add_i32 s49, s46, 1
	s_cmp_lg_u32 s46, 2
	s_cselect_b32 s46, s49, 0
	s_waitcnt lgkmcnt(0)
	s_setprio 1
	v_mfma_f32_16x16x32_f16 v[62:65], v[176:179], v[192:195], v[62:65]
	v_mfma_f32_16x16x32_f16 v[58:61], v[176:179], v[196:199], v[58:61]
	v_mfma_f32_16x16x32_f16 v[54:57], v[176:179], v[200:203], v[54:57]
	v_mfma_f32_16x16x32_f16 v[50:53], v[176:179], v[204:207], v[50:53]
	v_mfma_f32_16x16x32_f16 v[46:49], v[180:183], v[192:195], v[46:49]
	v_mfma_f32_16x16x32_f16 v[42:45], v[180:183], v[196:199], v[42:45]
	v_mfma_f32_16x16x32_f16 v[38:41], v[180:183], v[200:203], v[38:41]
	v_mfma_f32_16x16x32_f16 v[34:37], v[180:183], v[204:207], v[34:37]
	v_mfma_f32_16x16x32_f16 v[30:33], v[184:187], v[192:195], v[30:33]
	v_mfma_f32_16x16x32_f16 v[26:29], v[184:187], v[196:199], v[26:29]
	v_mfma_f32_16x16x32_f16 v[22:25], v[184:187], v[200:203], v[22:25]
	v_mfma_f32_16x16x32_f16 v[18:21], v[184:187], v[204:207], v[18:21]
	v_mfma_f32_16x16x32_f16 v[14:17], v[188:191], v[192:195], v[14:17]
	v_mfma_f32_16x16x32_f16 v[10:13], v[188:191], v[196:199], v[10:13]
	v_mfma_f32_16x16x32_f16 v[6:9], v[188:191], v[200:203], v[6:9]
	v_mfma_f32_16x16x32_f16 v[2:5], v[188:191], v[204:207], v[2:5]
	v_mfma_f32_16x16x32_f16 v[62:65], v[208:211], v[224:227], v[62:65]
	v_mfma_f32_16x16x32_f16 v[58:61], v[208:211], v[228:231], v[58:61]
	v_mfma_f32_16x16x32_f16 v[54:57], v[208:211], v[232:235], v[54:57]
	v_mfma_f32_16x16x32_f16 v[50:53], v[208:211], v[236:239], v[50:53]
	v_mfma_f32_16x16x32_f16 v[46:49], v[212:215], v[224:227], v[46:49]
	v_mfma_f32_16x16x32_f16 v[42:45], v[212:215], v[228:231], v[42:45]
	v_mfma_f32_16x16x32_f16 v[38:41], v[212:215], v[232:235], v[38:41]
	v_mfma_f32_16x16x32_f16 v[34:37], v[212:215], v[236:239], v[34:37]
	v_mfma_f32_16x16x32_f16 v[30:33], v[216:219], v[224:227], v[30:33]
	v_mfma_f32_16x16x32_f16 v[26:29], v[216:219], v[228:231], v[26:29]
	v_mfma_f32_16x16x32_f16 v[22:25], v[216:219], v[232:235], v[22:25]
	v_mfma_f32_16x16x32_f16 v[18:21], v[216:219], v[236:239], v[18:21]
	v_mfma_f32_16x16x32_f16 v[14:17], v[220:223], v[224:227], v[14:17]
	v_mfma_f32_16x16x32_f16 v[10:13], v[220:223], v[228:231], v[10:13]
	v_mfma_f32_16x16x32_f16 v[6:9], v[220:223], v[232:235], v[6:9]
	v_mfma_f32_16x16x32_f16 v[2:5], v[220:223], v[236:239], v[2:5]
	s_setprio 0
	s_branch .Lqk_epi_start

.Lqk_epi_start:
	s_barrier
	v_and_b32_e32 v66, 15, v0
	v_bfe_u32 v67, v0, 6, 2
	v_and_b32_e32 v68, 7, v66
	v_lshlrev_b32_e32 v68, 1, v68
	v_lshlrev_b32_e32 v70, 15, v78
	s_cmp_lt_i32 s20, 16
	s_cbranch_scc0 .Lqk_epi_swp
	s_mov_b32 s0, 1.0
	s_cmp_lt_i32 s20, 8
	s_cselect_b32 s0, 0x3e38aa3b, s0
	v_xor_b32_e32 v69, v1, v68
	v_lshl_or_b32 v70, v67, 13, v70
	v_lshl_or_b32 v70, v66, 7, v70
	v_xor_b32_e32 v71, 0, v69
	v_lshl_add_u32 v71, v71, 3, v70
	v_pk_add_f32 v[72:73], v[62:63], v[128:129]
	v_pk_add_f32 v[74:75], v[64:65], v[130:131]
	v_pk_mul_f32 v[72:73], v[72:73], s[0:1] op_sel_hi:[1,0]
	v_pk_mul_f32 v[74:75], v[74:75], s[0:1] op_sel_hi:[1,0]
	v_cvt_pk_f16_f32 v72, v72, v73
	v_cvt_pk_f16_f32 v73, v74, v75
	ds_write_b64 v71, v[72:73]
	v_pk_add_f32 v[80:81], v[58:59], v[128:129]
	v_pk_add_f32 v[82:83], v[60:61], v[130:131]
	v_pk_mul_f32 v[80:81], v[80:81], s[0:1] op_sel_hi:[1,0]
	v_pk_mul_f32 v[82:83], v[82:83], s[0:1] op_sel_hi:[1,0]
	v_cvt_pk_f16_f32 v80, v80, v81
	v_cvt_pk_f16_f32 v81, v82, v83
	ds_write_b64 v71, v[80:81] offset:2048
	v_pk_add_f32 v[72:73], v[54:55], v[128:129]
	v_pk_add_f32 v[74:75], v[56:57], v[130:131]
	v_pk_mul_f32 v[72:73], v[72:73], s[0:1] op_sel_hi:[1,0]
	v_pk_mul_f32 v[74:75], v[74:75], s[0:1] op_sel_hi:[1,0]
	v_cvt_pk_f16_f32 v72, v72, v73
	v_cvt_pk_f16_f32 v73, v74, v75
	ds_write_b64 v71, v[72:73] offset:4096
	v_pk_add_f32 v[80:81], v[50:51], v[128:129]
	v_pk_add_f32 v[82:83], v[52:53], v[130:131]
	v_pk_mul_f32 v[80:81], v[80:81], s[0:1] op_sel_hi:[1,0]
	v_pk_mul_f32 v[82:83], v[82:83], s[0:1] op_sel_hi:[1,0]
	v_cvt_pk_f16_f32 v80, v80, v81
	v_cvt_pk_f16_f32 v81, v82, v83
	ds_write_b64 v71, v[80:81] offset:6144
	v_xor_b32_e32 v71, 4, v69
	v_lshl_add_u32 v71, v71, 3, v70
	v_pk_add_f32 v[72:73], v[46:47], v[132:133]
	v_pk_add_f32 v[74:75], v[48:49], v[134:135]
	v_pk_mul_f32 v[72:73], v[72:73], s[0:1] op_sel_hi:[1,0]
	v_pk_mul_f32 v[74:75], v[74:75], s[0:1] op_sel_hi:[1,0]
	v_cvt_pk_f16_f32 v72, v72, v73
	v_cvt_pk_f16_f32 v73, v74, v75
	ds_write_b64 v71, v[72:73]
	v_pk_add_f32 v[80:81], v[42:43], v[132:133]
	v_pk_add_f32 v[82:83], v[44:45], v[134:135]
	v_pk_mul_f32 v[80:81], v[80:81], s[0:1] op_sel_hi:[1,0]
	v_pk_mul_f32 v[82:83], v[82:83], s[0:1] op_sel_hi:[1,0]
	v_cvt_pk_f16_f32 v80, v80, v81
	v_cvt_pk_f16_f32 v81, v82, v83
	ds_write_b64 v71, v[80:81] offset:2048
	v_pk_add_f32 v[72:73], v[38:39], v[132:133]
	v_pk_add_f32 v[74:75], v[40:41], v[134:135]
	v_pk_mul_f32 v[72:73], v[72:73], s[0:1] op_sel_hi:[1,0]
	v_pk_mul_f32 v[74:75], v[74:75], s[0:1] op_sel_hi:[1,0]
	v_cvt_pk_f16_f32 v72, v72, v73
	v_cvt_pk_f16_f32 v73, v74, v75
	ds_write_b64 v71, v[72:73] offset:4096
	v_pk_add_f32 v[80:81], v[34:35], v[132:133]
	v_pk_add_f32 v[82:83], v[36:37], v[134:135]
	v_pk_mul_f32 v[80:81], v[80:81], s[0:1] op_sel_hi:[1,0]
	v_pk_mul_f32 v[82:83], v[82:83], s[0:1] op_sel_hi:[1,0]
	v_cvt_pk_f16_f32 v80, v80, v81
	v_cvt_pk_f16_f32 v81, v82, v83
	ds_write_b64 v71, v[80:81] offset:6144
	v_xor_b32_e32 v71, 8, v69
	v_lshl_add_u32 v71, v71, 3, v70
	v_pk_add_f32 v[72:73], v[30:31], v[136:137]
	v_pk_add_f32 v[74:75], v[32:33], v[138:139]
	v_pk_mul_f32 v[72:73], v[72:73], s[0:1] op_sel_hi:[1,0]
	v_pk_mul_f32 v[74:75], v[74:75], s[0:1] op_sel_hi:[1,0]
	v_cvt_pk_f16_f32 v72, v72, v73
	v_cvt_pk_f16_f32 v73, v74, v75
	ds_write_b64 v71, v[72:73]
	v_pk_add_f32 v[80:81], v[26:27], v[136:137]
	v_pk_add_f32 v[82:83], v[28:29], v[138:139]
	v_pk_mul_f32 v[80:81], v[80:81], s[0:1] op_sel_hi:[1,0]
	v_pk_mul_f32 v[82:83], v[82:83], s[0:1] op_sel_hi:[1,0]
	v_cvt_pk_f16_f32 v80, v80, v81
	v_cvt_pk_f16_f32 v81, v82, v83
	ds_write_b64 v71, v[80:81] offset:2048
	v_pk_add_f32 v[72:73], v[22:23], v[136:137]
	v_pk_add_f32 v[74:75], v[24:25], v[138:139]
	v_pk_mul_f32 v[72:73], v[72:73], s[0:1] op_sel_hi:[1,0]
	v_pk_mul_f32 v[74:75], v[74:75], s[0:1] op_sel_hi:[1,0]
	v_cvt_pk_f16_f32 v72, v72, v73
	v_cvt_pk_f16_f32 v73, v74, v75
	ds_write_b64 v71, v[72:73] offset:4096
	v_pk_add_f32 v[80:81], v[18:19], v[136:137]
	v_pk_add_f32 v[82:83], v[20:21], v[138:139]
	v_pk_mul_f32 v[80:81], v[80:81], s[0:1] op_sel_hi:[1,0]
	v_pk_mul_f32 v[82:83], v[82:83], s[0:1] op_sel_hi:[1,0]
	v_cvt_pk_f16_f32 v80, v80, v81
	v_cvt_pk_f16_f32 v81, v82, v83
	ds_write_b64 v71, v[80:81] offset:6144
	v_xor_b32_e32 v71, 12, v69
	v_lshl_add_u32 v71, v71, 3, v70
	v_pk_add_f32 v[72:73], v[14:15], v[140:141]
	v_pk_add_f32 v[74:75], v[16:17], v[142:143]
	v_pk_mul_f32 v[72:73], v[72:73], s[0:1] op_sel_hi:[1,0]
	v_pk_mul_f32 v[74:75], v[74:75], s[0:1] op_sel_hi:[1,0]
	v_cvt_pk_f16_f32 v72, v72, v73
	v_cvt_pk_f16_f32 v73, v74, v75
	ds_write_b64 v71, v[72:73]
	v_pk_add_f32 v[80:81], v[10:11], v[140:141]
	v_pk_add_f32 v[82:83], v[12:13], v[142:143]
	v_pk_mul_f32 v[80:81], v[80:81], s[0:1] op_sel_hi:[1,0]
	v_pk_mul_f32 v[82:83], v[82:83], s[0:1] op_sel_hi:[1,0]
	v_cvt_pk_f16_f32 v80, v80, v81
	v_cvt_pk_f16_f32 v81, v82, v83
	ds_write_b64 v71, v[80:81] offset:2048
	v_pk_add_f32 v[72:73], v[6:7], v[140:141]
	v_pk_add_f32 v[74:75], v[8:9], v[142:143]
	v_pk_mul_f32 v[72:73], v[72:73], s[0:1] op_sel_hi:[1,0]
	v_pk_mul_f32 v[74:75], v[74:75], s[0:1] op_sel_hi:[1,0]
	v_cvt_pk_f16_f32 v72, v72, v73
	v_cvt_pk_f16_f32 v73, v74, v75
	ds_write_b64 v71, v[72:73] offset:4096
	v_pk_add_f32 v[80:81], v[2:3], v[140:141]
	v_pk_add_f32 v[82:83], v[4:5], v[142:143]
	v_pk_mul_f32 v[80:81], v[80:81], s[0:1] op_sel_hi:[1,0]
	v_pk_mul_f32 v[82:83], v[82:83], s[0:1] op_sel_hi:[1,0]
	v_cvt_pk_f16_f32 v80, v80, v81
	v_cvt_pk_f16_f32 v81, v82, v83
	ds_write_b64 v71, v[80:81] offset:6144
	s_branch .Lqk_epi_join

	.amdhsa_kernel _Z12gemm1_kernel6G1Args
		.amdhsa_group_segment_fixed_size 163840
		.amdhsa_private_segment_fixed_size 0
		.amdhsa_kernarg_size 88
		.amdhsa_user_sgpr_count 2
		.amdhsa_user_sgpr_dispatch_ptr 0
		.amdhsa_user_sgpr_queue_ptr 0
		.amdhsa_user_sgpr_kernarg_segment_ptr 1
		.amdhsa_user_sgpr_dispatch_id 0
		.amdhsa_user_sgpr_kernarg_preload_length 0
		.amdhsa_user_sgpr_kernarg_preload_offset 0
		.amdhsa_user_sgpr_private_segment_size 0
		.amdhsa_uses_dynamic_stack 0
		.amdhsa_enable_private_segment 0
		.amdhsa_system_sgpr_workgroup_id_x 1
		.amdhsa_system_sgpr_workgroup_id_y 0
		.amdhsa_system_sgpr_workgroup_id_z 0
		.amdhsa_system_sgpr_workgroup_info 0
		.amdhsa_system_vgpr_workitem_id 0
		.amdhsa_next_free_vgpr 240
		.amdhsa_next_free_sgpr 96
		.amdhsa_accum_offset 240
		.amdhsa_reserve_vcc 1
		.amdhsa_float_round_mode_32 0
		.amdhsa_float_round_mode_16_64 0
		.amdhsa_float_denorm_mode_32 3
		.amdhsa_float_denorm_mode_16_64 3
		.amdhsa_dx10_clamp 1
		.amdhsa_ieee_mode 1
		.amdhsa_fp16_overflow 0
		.amdhsa_tg_split 0
		.amdhsa_exception_fp_ieee_invalid_op 0
		.amdhsa_exception_fp_denorm_src 0
		.amdhsa_exception_fp_ieee_div_zero 0
		.amdhsa_exception_fp_ieee_overflow 0
		.amdhsa_exception_fp_ieee_underflow 0
		.amdhsa_exception_fp_ieee_inexact 0
		.amdhsa_exception_int_div_zero 0
	.end_amdhsa_kernel

amdhsa.kernels:
  - .agpr_count:     0
    .args:
      - .actual_access:  read_only
        .address_space:  global
        .offset:         0
        .size:           8
        .value_kind:     global_buffer
      - .actual_access:  read_only
        .address_space:  global
        .offset:         8
        .size:           8
        .value_kind:     global_buffer
      - .actual_access:  read_only
        .address_space:  global
        .offset:         16
        .size:           8
        .value_kind:     global_buffer
      - .actual_access:  read_only
        .address_space:  global
        .offset:         24
        .size:           8
        .value_kind:     global_buffer
      - .actual_access:  read_only
        .address_space:  global
        .offset:         32
        .size:           8
        .value_kind:     global_buffer
      - .actual_access:  read_only
        .address_space:  global
        .offset:         40
        .size:           8
        .value_kind:     global_buffer
      - .actual_access:  read_only
        .address_space:  global
        .offset:         48
        .size:           8
        .value_kind:     global_buffer
      - .address_space:  global
        .offset:         56
        .size:           8
        .value_kind:     global_buffer
      - .address_space:  global
        .offset:         64
        .size:           8
        .value_kind:     global_buffer
      - .actual_access:  read_only
        .address_space:  global
        .offset:         72
        .size:           8
        .value_kind:     global_buffer
      - .address_space:  global
        .offset:         80
        .size:           8
        .value_kind:     global_buffer
    .group_segment_fixed_size: 0
    .kernarg_segment_align: 8
    .kernarg_segment_size: 88
    .language:       OpenCL C
    .language_version:
      - 2
      - 0
    .max_flat_workgroup_size: 256
    .name:           _Z11prep_kernelPKfS0_S0_S0_S0_S0_S0_PDF16_S1_S1_S1_
    .private_segment_fixed_size: 0
    .sgpr_count:     23
    .sgpr_spill_count: 0
    .symbol:         _Z11prep_kernelPKfS0_S0_S0_S0_S0_S0_PDF16_S1_S1_S1_.kd
    .uniform_work_group_size: 1
    .uses_dynamic_stack: false
    .vgpr_count:     28
    .vgpr_spill_count: 0
    .wavefront_size: 64
  - .agpr_count:     0
    .args:
      - .offset:         0
        .size:           88
        .value_kind:     by_value
    .group_segment_fixed_size: 163840
    .kernarg_segment_align: 8
    .kernarg_segment_size: 88
    .language:       OpenCL C
    .language_version:
      - 2
      - 0
    .max_flat_workgroup_size: 512
    .name:           _Z12gemm1_kernel6G1Args
    .private_segment_fixed_size: 0
    .sgpr_count:     58
    .sgpr_spill_count: 0
    .symbol:         _Z12gemm1_kernel6G1Args.kd
    .uniform_work_group_size: 1
    .uses_dynamic_stack: false
    .vgpr_count:     240
    .vgpr_spill_count: 0
    .wavefront_size: 64
  - .agpr_count:     0
    .args:
      - .address_space:  global
        .offset:         0
        .size:           8
        .value_kind:     global_buffer
      - .address_space:  global
        .offset:         8
        .size:           8
        .value_kind:     global_buffer
      - .address_space:  global
        .offset:         16
        .size:           8
        .value_kind:     global_buffer
      - .actual_access:  read_only
        .address_space:  global
        .offset:         24
        .size:           8
        .value_kind:     global_buffer
      - .actual_access:  read_only
        .address_space:  global
        .offset:         32
        .size:           8
        .value_kind:     global_buffer
      - .actual_access:  read_only
        .address_space:  global
        .offset:         40
        .size:           8
        .value_kind:     global_buffer
      - .address_space:  global
        .offset:         48
        .size:           8
        .value_kind:     global_buffer
      - .actual_access:  read_only
        .address_space:  global
        .offset:         56
        .size:           8
        .value_kind:     global_buffer
      - .address_space:  global
        .offset:         64
        .size:           8
        .value_kind:     global_buffer
      - .actual_access:  read_only
        .address_space:  global
        .offset:         72
        .size:           8
        .value_kind:     global_buffer
      - .address_space:  global
        .offset:         80
        .size:           8
        .value_kind:     global_buffer
    .group_segment_fixed_size: 81920
    .kernarg_segment_align: 8
    .kernarg_segment_size: 88
    .language:       OpenCL C
    .language_version:
      - 2
      - 0
    .max_flat_workgroup_size: 512
    .name:           _Z11attn_kernelPKDF16_S0_S0_PKfS2_S2_S0_S2_PDF16_S2_S3_
    .private_segment_fixed_size: 0
    .sgpr_count:     62
    .sgpr_spill_count: 0
    .symbol:         _Z11attn_kernelPKDF16_S0_S0_PKfS2_S2_S0_S2_PDF16_S2_S3_.kd
    .uniform_work_group_size: 1
    .uses_dynamic_stack: false
    .vgpr_count:     126
    .vgpr_spill_count: 0
    .wavefront_size: 64
  - .agpr_count:     0
    .args:
      - .address_space:  global
        .offset:         0
        .size:           8
        .value_kind:     global_buffer
      - .address_space:  global
        .offset:         8
        .size:           8
        .value_kind:     global_buffer
      - .actual_access:  read_only
        .address_space:  global
        .offset:         16
        .size:           8
        .value_kind:     global_buffer
      - .actual_access:  write_only
        .address_space:  global
        .offset:         24
        .size:           8
        .value_kind:     global_buffer
    .group_segment_fixed_size: 122880
    .kernarg_segment_align: 8
    .kernarg_segment_size: 32
    .language:       OpenCL C
    .language_version:
      - 2
      - 0
    .max_flat_workgroup_size: 512
    .name:           _Z14outproj_kernelPKDF16_S0_PKfPf
    .private_segment_fixed_size: 0
    .sgpr_count:     31
    .sgpr_spill_count: 0
    .symbol:         _Z14outproj_kernelPKDF16_S0_PKfPf.kd
    .uniform_work_group_size: 1
    .uses_dynamic_stack: false
    .vgpr_count:     132
    .vgpr_spill_count: 0
    .wavefront_size: 64
